# SGPR-base LDS-DMA loads (no VALU address adds) extended to the LRU-gate and MoE-down GEMM main K loops of both layers (generic converter), on top of the proj loops
# baseline (speedup 1.0000x reference)
.LBB0_271:
	ds_read_b128 v[158:161], v153
	ds_read_b128 v[162:165], v153 offset:1024
	ds_read_b128 v[166:169], v153 offset:2048
	ds_read_b128 v[170:173], v153 offset:3072
	ds_read_b128 v[174:177], v154
	ds_read_b128 v[178:181], v154 offset:1024
	ds_read_b128 v[182:185], v154 offset:2048
	ds_read_b128 v[186:189], v154 offset:3072
	s_add_u32 s30, s28, 0xfffc0080
	s_addc_u32 s31, s29, -1
	s_cmp_eq_u32 s65, 12
	s_cselect_b32 s35, s23, s31
	s_cselect_b32 s34, s22, s30
	s_cselect_b32 s31, s25, s64
	s_cselect_b32 s30, s24, s63
	s_mov_b32 m0, s19
	ds_read_b128 v[190:193], v155
	ds_read_b128 v[194:197], v155 offset:1024
	ds_read_b128 v[198:201], v155 offset:2048
	ds_read_b128 v[202:205], v155 offset:3072
	ds_read_b128 v[206:209], v155 offset:4096
	ds_read_b128 v[210:213], v155 offset:5120
	ds_read_b128 v[214:217], v155 offset:6144
	ds_read_b128 v[218:221], v155 offset:7168
	global_load_lds_dwordx4 v144, s[28:29]
	s_mov_b32 m0, s21
	s_nop 0
	global_load_lds_dwordx4 v142, s[28:29]
	s_waitcnt vmcnt(8)
	s_waitcnt lgkmcnt(0)
	s_barrier
	s_setprio 1
	s_waitcnt lgkmcnt(0)
	v_mfma_f32_16x16x32_bf16 v[116:119], v[158:161], v[190:193], v[116:119]
	v_mfma_f32_16x16x32_bf16 v[112:115], v[166:169], v[190:193], v[112:115]
	v_mfma_f32_16x16x32_bf16 v[100:103], v[158:161], v[198:201], v[100:103]
	v_mfma_f32_16x16x32_bf16 v[96:99], v[166:169], v[198:201], v[96:99]
	v_mfma_f32_16x16x32_bf16 v[84:87], v[158:161], v[206:209], v[84:87]
	v_mfma_f32_16x16x32_bf16 v[80:83], v[166:169], v[206:209], v[80:83]
	v_mfma_f32_16x16x32_bf16 v[68:71], v[158:161], v[214:217], v[68:71]
	v_mfma_f32_16x16x32_bf16 v[64:67], v[166:169], v[214:217], v[64:67]
	v_mfma_f32_16x16x32_bf16 v[116:119], v[162:165], v[194:197], v[116:119]
	v_mfma_f32_16x16x32_bf16 v[112:115], v[170:173], v[194:197], v[112:115]
	v_mfma_f32_16x16x32_bf16 v[100:103], v[162:165], v[202:205], v[100:103]
	v_mfma_f32_16x16x32_bf16 v[96:99], v[170:173], v[202:205], v[96:99]
	v_mfma_f32_16x16x32_bf16 v[84:87], v[162:165], v[210:213], v[84:87]
	v_mfma_f32_16x16x32_bf16 v[80:83], v[170:173], v[210:213], v[80:83]
	v_mfma_f32_16x16x32_bf16 v[68:71], v[162:165], v[218:221], v[68:71]
	v_mfma_f32_16x16x32_bf16 v[64:67], v[170:173], v[218:221], v[64:67]
	s_setprio 0
	s_setprio 1
	v_mfma_f32_16x16x32_bf16 v[124:127], v[174:177], v[190:193], v[124:127]
	v_mfma_f32_16x16x32_bf16 v[120:123], v[182:185], v[190:193], v[120:123]
	v_mfma_f32_16x16x32_bf16 v[108:111], v[174:177], v[198:201], v[108:111]
	v_mfma_f32_16x16x32_bf16 v[104:107], v[182:185], v[198:201], v[104:107]
	v_mfma_f32_16x16x32_bf16 v[92:95], v[174:177], v[206:209], v[92:95]
	v_mfma_f32_16x16x32_bf16 v[88:91], v[182:185], v[206:209], v[88:91]
	v_mfma_f32_16x16x32_bf16 v[76:79], v[174:177], v[214:217], v[76:79]
	v_mfma_f32_16x16x32_bf16 v[72:75], v[182:185], v[214:217], v[72:75]
	v_mfma_f32_16x16x32_bf16 v[124:127], v[178:181], v[194:197], v[124:127]
	v_mfma_f32_16x16x32_bf16 v[120:123], v[186:189], v[194:197], v[120:123]
	v_mfma_f32_16x16x32_bf16 v[108:111], v[178:181], v[202:205], v[108:111]
	v_mfma_f32_16x16x32_bf16 v[104:107], v[186:189], v[202:205], v[104:107]
	v_mfma_f32_16x16x32_bf16 v[92:95], v[178:181], v[210:213], v[92:95]
	v_mfma_f32_16x16x32_bf16 v[88:91], v[186:189], v[210:213], v[88:91]
	v_mfma_f32_16x16x32_bf16 v[76:79], v[178:181], v[218:221], v[76:79]
	v_mfma_f32_16x16x32_bf16 v[72:75], v[186:189], v[218:221], v[72:75]
	s_setprio 0
	s_barrier
	s_mov_b32 m0, s55
	s_add_u32 s66, s30, 0x40000
	ds_read_b128 v[190:193], v155 offset:16384
	ds_read_b128 v[194:197], v155 offset:17408
	ds_read_b128 v[198:201], v155 offset:18432
	ds_read_b128 v[202:205], v155 offset:19456
	ds_read_b128 v[206:209], v155 offset:20480
	ds_read_b128 v[210:213], v155 offset:21504
	ds_read_b128 v[214:217], v155 offset:22528
	ds_read_b128 v[218:221], v155 offset:23552
	global_load_lds_dwordx4 v132, s[30:31]
	s_mov_b32 m0, s56
	s_addc_u32 s67, s31, 0
	global_load_lds_dwordx4 v128, s[30:31]
	s_mov_b32 m0, s57
	s_nop 0
	global_load_lds_dwordx4 v132, s[66:67]
	s_mov_b32 m0, s58
	s_nop 0
	global_load_lds_dwordx4 v128, s[66:67]
	s_mov_b32 m0, s43
	s_nop 0
	global_load_lds_dwordx4 v134, s[34:35]
	s_mov_b32 m0, s44
	s_nop 0
	global_load_lds_dwordx4 v130, s[34:35]
	s_waitcnt vmcnt(8)
	s_waitcnt lgkmcnt(0)
	s_barrier
	s_setprio 1
	s_waitcnt lgkmcnt(0)
	v_mfma_f32_16x16x32_bf16 v[52:55], v[158:161], v[190:193], v[52:55]
	v_mfma_f32_16x16x32_bf16 v[48:51], v[166:169], v[190:193], v[48:51]
	v_mfma_f32_16x16x32_bf16 v[36:39], v[158:161], v[198:201], v[36:39]
	v_mfma_f32_16x16x32_bf16 v[32:35], v[166:169], v[198:201], v[32:35]
	v_mfma_f32_16x16x32_bf16 v[20:23], v[158:161], v[206:209], v[20:23]
	v_mfma_f32_16x16x32_bf16 v[16:19], v[166:169], v[206:209], v[16:19]
	v_mfma_f32_16x16x32_bf16 v[4:7], v[158:161], v[214:217], v[4:7]
	v_mfma_f32_16x16x32_bf16 v[0:3], v[166:169], v[214:217], v[0:3]
	v_mfma_f32_16x16x32_bf16 v[52:55], v[162:165], v[194:197], v[52:55]
	v_mfma_f32_16x16x32_bf16 v[48:51], v[170:173], v[194:197], v[48:51]
	v_mfma_f32_16x16x32_bf16 v[36:39], v[162:165], v[202:205], v[36:39]
	v_mfma_f32_16x16x32_bf16 v[32:35], v[170:173], v[202:205], v[32:35]
	v_mfma_f32_16x16x32_bf16 v[20:23], v[162:165], v[210:213], v[20:23]
	v_mfma_f32_16x16x32_bf16 v[16:19], v[170:173], v[210:213], v[16:19]
	v_mfma_f32_16x16x32_bf16 v[4:7], v[162:165], v[218:221], v[4:7]
	v_mfma_f32_16x16x32_bf16 v[0:3], v[170:173], v[218:221], v[0:3]
	s_setprio 0
	s_setprio 1
	v_mfma_f32_16x16x32_bf16 v[60:63], v[174:177], v[190:193], v[60:63]
	v_mfma_f32_16x16x32_bf16 v[56:59], v[182:185], v[190:193], v[56:59]
	v_mfma_f32_16x16x32_bf16 v[44:47], v[174:177], v[198:201], v[44:47]
	v_mfma_f32_16x16x32_bf16 v[40:43], v[182:185], v[198:201], v[40:43]
	v_mfma_f32_16x16x32_bf16 v[28:31], v[174:177], v[206:209], v[28:31]
	v_mfma_f32_16x16x32_bf16 v[24:27], v[182:185], v[206:209], v[24:27]
	v_mfma_f32_16x16x32_bf16 v[12:15], v[174:177], v[214:217], v[12:15]
	v_mfma_f32_16x16x32_bf16 v[8:11], v[182:185], v[214:217], v[8:11]
	v_mfma_f32_16x16x32_bf16 v[60:63], v[178:181], v[194:197], v[60:63]
	v_mfma_f32_16x16x32_bf16 v[56:59], v[186:189], v[194:197], v[56:59]
	v_mfma_f32_16x16x32_bf16 v[44:47], v[178:181], v[202:205], v[44:47]
	v_mfma_f32_16x16x32_bf16 v[40:43], v[186:189], v[202:205], v[40:43]
	v_mfma_f32_16x16x32_bf16 v[28:31], v[178:181], v[210:213], v[28:31]
	v_mfma_f32_16x16x32_bf16 v[24:27], v[186:189], v[210:213], v[24:27]
	v_mfma_f32_16x16x32_bf16 v[12:15], v[178:181], v[218:221], v[12:15]
	v_mfma_f32_16x16x32_bf16 v[8:11], v[186:189], v[218:221], v[8:11]
	s_setprio 0
	s_barrier
	ds_read_b128 v[158:161], v136
	ds_read_b128 v[162:165], v136 offset:1024
	ds_read_b128 v[166:169], v136 offset:2048
	ds_read_b128 v[170:173], v136 offset:3072
	ds_read_b128 v[174:177], v157
	ds_read_b128 v[178:181], v157 offset:1024
	ds_read_b128 v[182:185], v157 offset:2048
	ds_read_b128 v[186:189], v157 offset:3072
	s_add_u32 s100, s34, 0x80
	s_addc_u32 s101, s35, 0
	s_add_u32 s34, s34, 0x40000
	s_addc_u32 s35, s35, 0
	s_mov_b32 m0, s45
	ds_read_b128 v[190:193], v155 offset:32768
	ds_read_b128 v[194:197], v155 offset:33792
	ds_read_b128 v[198:201], v155 offset:34816
	ds_read_b128 v[202:205], v155 offset:35840
	ds_read_b128 v[206:209], v155 offset:36864
	ds_read_b128 v[210:213], v155 offset:37888
	ds_read_b128 v[214:217], v155 offset:38912
	ds_read_b128 v[218:221], v155 offset:39936
	global_load_lds_dwordx4 v134, s[34:35]
	s_mov_b32 m0, s46
	s_nop 0
	global_load_lds_dwordx4 v130, s[34:35]
	s_waitcnt vmcnt(8)
	s_waitcnt lgkmcnt(0)
	s_barrier
	s_setprio 1
	s_waitcnt lgkmcnt(0)
	v_mfma_f32_16x16x32_bf16 v[116:119], v[158:161], v[190:193], v[116:119]
	v_mfma_f32_16x16x32_bf16 v[112:115], v[166:169], v[190:193], v[112:115]
	v_mfma_f32_16x16x32_bf16 v[100:103], v[158:161], v[198:201], v[100:103]
	v_mfma_f32_16x16x32_bf16 v[96:99], v[166:169], v[198:201], v[96:99]
	v_mfma_f32_16x16x32_bf16 v[84:87], v[158:161], v[206:209], v[84:87]
	v_mfma_f32_16x16x32_bf16 v[80:83], v[166:169], v[206:209], v[80:83]
	v_mfma_f32_16x16x32_bf16 v[68:71], v[158:161], v[214:217], v[68:71]
	v_mfma_f32_16x16x32_bf16 v[64:67], v[166:169], v[214:217], v[64:67]
	v_mfma_f32_16x16x32_bf16 v[116:119], v[162:165], v[194:197], v[116:119]
	v_mfma_f32_16x16x32_bf16 v[112:115], v[170:173], v[194:197], v[112:115]
	v_mfma_f32_16x16x32_bf16 v[100:103], v[162:165], v[202:205], v[100:103]
	v_mfma_f32_16x16x32_bf16 v[96:99], v[170:173], v[202:205], v[96:99]
	v_mfma_f32_16x16x32_bf16 v[84:87], v[162:165], v[210:213], v[84:87]
	v_mfma_f32_16x16x32_bf16 v[80:83], v[170:173], v[210:213], v[80:83]
	v_mfma_f32_16x16x32_bf16 v[68:71], v[162:165], v[218:221], v[68:71]
	v_mfma_f32_16x16x32_bf16 v[64:67], v[170:173], v[218:221], v[64:67]
	s_setprio 0
	s_setprio 1
	v_mfma_f32_16x16x32_bf16 v[124:127], v[174:177], v[190:193], v[124:127]
	v_mfma_f32_16x16x32_bf16 v[120:123], v[182:185], v[190:193], v[120:123]
	v_mfma_f32_16x16x32_bf16 v[108:111], v[174:177], v[198:201], v[108:111]
	v_mfma_f32_16x16x32_bf16 v[104:107], v[182:185], v[198:201], v[104:107]
	v_mfma_f32_16x16x32_bf16 v[92:95], v[174:177], v[206:209], v[92:95]
	v_mfma_f32_16x16x32_bf16 v[88:91], v[182:185], v[206:209], v[88:91]
	v_mfma_f32_16x16x32_bf16 v[76:79], v[174:177], v[214:217], v[76:79]
	v_mfma_f32_16x16x32_bf16 v[72:75], v[182:185], v[214:217], v[72:75]
	v_mfma_f32_16x16x32_bf16 v[124:127], v[178:181], v[194:197], v[124:127]
	v_mfma_f32_16x16x32_bf16 v[120:123], v[186:189], v[194:197], v[120:123]
	v_mfma_f32_16x16x32_bf16 v[108:111], v[178:181], v[202:205], v[108:111]
	v_mfma_f32_16x16x32_bf16 v[104:107], v[186:189], v[202:205], v[104:107]
	v_mfma_f32_16x16x32_bf16 v[92:95], v[178:181], v[210:213], v[92:95]
	v_mfma_f32_16x16x32_bf16 v[88:91], v[186:189], v[210:213], v[88:91]
	v_mfma_f32_16x16x32_bf16 v[76:79], v[178:181], v[218:221], v[76:79]
	v_mfma_f32_16x16x32_bf16 v[72:75], v[186:189], v[218:221], v[72:75]
	s_setprio 0
	s_barrier
	s_mov_b32 m0, s59
	s_add_u32 s98, s30, 0x80
	s_addc_u32 s99, s31, 0
	s_add_u32 s30, s30, 0x40080
	ds_read_b128 v[190:193], v155 offset:49152
	ds_read_b128 v[194:197], v155 offset:50176
	ds_read_b128 v[198:201], v155 offset:51200
	ds_read_b128 v[202:205], v155 offset:52224
	ds_read_b128 v[206:209], v155 offset:53248
	ds_read_b128 v[210:213], v155 offset:54272
	ds_read_b128 v[214:217], v155 offset:55296
	ds_read_b128 v[218:221], v155 offset:56320
	global_load_lds_dwordx4 v132, s[98:99]
	s_mov_b32 m0, s60
	s_addc_u32 s31, s31, 0
	global_load_lds_dwordx4 v128, s[98:99]
	s_mov_b32 m0, s61
	s_nop 0
	global_load_lds_dwordx4 v132, s[30:31]
	s_mov_b32 m0, s62
	s_nop 0
	global_load_lds_dwordx4 v128, s[30:31]
	s_mov_b32 m0, s48
	s_nop 0
	global_load_lds_dwordx4 v134, s[100:101]
	s_mov_b32 m0, s49
	s_nop 0
	global_load_lds_dwordx4 v130, s[100:101]
	s_waitcnt vmcnt(8)
	s_waitcnt lgkmcnt(0)
	s_barrier
	s_setprio 1
	s_waitcnt lgkmcnt(0)
	v_mfma_f32_16x16x32_bf16 v[52:55], v[158:161], v[190:193], v[52:55]
	v_mfma_f32_16x16x32_bf16 v[48:51], v[166:169], v[190:193], v[48:51]
	v_mfma_f32_16x16x32_bf16 v[36:39], v[158:161], v[198:201], v[36:39]
	v_mfma_f32_16x16x32_bf16 v[32:35], v[166:169], v[198:201], v[32:35]
	v_mfma_f32_16x16x32_bf16 v[20:23], v[158:161], v[206:209], v[20:23]
	v_mfma_f32_16x16x32_bf16 v[16:19], v[166:169], v[206:209], v[16:19]
	v_mfma_f32_16x16x32_bf16 v[4:7], v[158:161], v[214:217], v[4:7]
	v_mfma_f32_16x16x32_bf16 v[0:3], v[166:169], v[214:217], v[0:3]
	v_mfma_f32_16x16x32_bf16 v[52:55], v[162:165], v[194:197], v[52:55]
	v_mfma_f32_16x16x32_bf16 v[48:51], v[170:173], v[194:197], v[48:51]
	v_mfma_f32_16x16x32_bf16 v[36:39], v[162:165], v[202:205], v[36:39]
	v_mfma_f32_16x16x32_bf16 v[32:35], v[170:173], v[202:205], v[32:35]
	v_mfma_f32_16x16x32_bf16 v[20:23], v[162:165], v[210:213], v[20:23]
	v_mfma_f32_16x16x32_bf16 v[16:19], v[170:173], v[210:213], v[16:19]
	v_mfma_f32_16x16x32_bf16 v[4:7], v[162:165], v[218:221], v[4:7]
	v_mfma_f32_16x16x32_bf16 v[0:3], v[170:173], v[218:221], v[0:3]
	s_setprio 0
	s_setprio 1
	v_mfma_f32_16x16x32_bf16 v[60:63], v[174:177], v[190:193], v[60:63]
	v_mfma_f32_16x16x32_bf16 v[56:59], v[182:185], v[190:193], v[56:59]
	v_mfma_f32_16x16x32_bf16 v[44:47], v[174:177], v[198:201], v[44:47]
	v_mfma_f32_16x16x32_bf16 v[40:43], v[182:185], v[198:201], v[40:43]
	v_mfma_f32_16x16x32_bf16 v[28:31], v[174:177], v[206:209], v[28:31]
	v_mfma_f32_16x16x32_bf16 v[24:27], v[182:185], v[206:209], v[24:27]
	v_mfma_f32_16x16x32_bf16 v[12:15], v[174:177], v[214:217], v[12:15]
	v_mfma_f32_16x16x32_bf16 v[8:11], v[182:185], v[214:217], v[8:11]
	v_mfma_f32_16x16x32_bf16 v[60:63], v[178:181], v[194:197], v[60:63]
	v_mfma_f32_16x16x32_bf16 v[56:59], v[186:189], v[194:197], v[56:59]
	v_mfma_f32_16x16x32_bf16 v[44:47], v[178:181], v[202:205], v[44:47]
	v_mfma_f32_16x16x32_bf16 v[40:43], v[186:189], v[202:205], v[40:43]
	v_mfma_f32_16x16x32_bf16 v[28:31], v[178:181], v[210:213], v[28:31]
	v_mfma_f32_16x16x32_bf16 v[24:27], v[186:189], v[210:213], v[24:27]
	v_mfma_f32_16x16x32_bf16 v[12:15], v[178:181], v[218:221], v[12:15]
	v_mfma_f32_16x16x32_bf16 v[8:11], v[186:189], v[218:221], v[8:11]
	s_setprio 0
	s_barrier
	s_add_i32 s65, s65, 2
	s_add_u32 s63, s63, 0x100
	s_addc_u32 s64, s64, 0
	s_add_u32 s28, s28, 0x100
	s_addc_u32 s29, s29, 0
	s_cmp_gt_u32 s65, 13
	s_cbranch_scc0 .LBB0_271
	s_and_b64 vcc, exec, s[12:13]
	s_cbranch_vccz .LBB0_274
	s_barrier

.LBB0_811:
	ds_read_b128 v[40:43], v231
	ds_read_b128 v[52:55], v231 offset:1024
	ds_read_b128 v[64:67], v231 offset:2048
	ds_read_b128 v[76:79], v231 offset:3072
	ds_read_b128 v[88:91], v232
	ds_read_b128 v[100:103], v232 offset:1024
	ds_read_b128 v[112:115], v232 offset:2048
	ds_read_b128 v[124:127], v232 offset:3072
	s_add_u32 s48, s46, 0xfffc0080
	s_addc_u32 s49, s47, -1
	s_cmp_eq_u32 s79, 12
	s_cselect_b32 s51, s7, s49
	s_cselect_b32 s50, s41, s48
	s_cselect_b32 s49, s43, s78
	s_cselect_b32 s48, s52, s53
	s_add_i32 m0, s64, 0xc000
	ds_read_b128 v[136:139], v233
	ds_read_b128 v[148:151], v233 offset:1024
	ds_read_b128 v[160:163], v233 offset:2048
	ds_read_b128 v[164:167], v233 offset:3072
	ds_read_b128 v[176:179], v233 offset:4096
	ds_read_b128 v[180:183], v233 offset:5120
	ds_read_b128 v[184:187], v233 offset:6144
	ds_read_b128 v[200:203], v233 offset:7168
	global_load_lds_dwordx4 v198, s[46:47]
	s_add_i32 m0, s64, 0xe000
	s_nop 0
	global_load_lds_dwordx4 v196, s[46:47]
	s_waitcnt vmcnt(8)
	s_waitcnt lgkmcnt(0)
	s_barrier
	s_setprio 1
	s_waitcnt lgkmcnt(0)
	v_mfma_f32_16x16x32_bf16 v[172:175], v[40:43], v[136:139], v[172:175]
	v_mfma_f32_16x16x32_bf16 v[168:171], v[64:67], v[136:139], v[168:171]
	v_mfma_f32_16x16x32_bf16 v[144:147], v[40:43], v[160:163], v[144:147]
	v_mfma_f32_16x16x32_bf16 v[140:143], v[64:67], v[160:163], v[140:143]
	v_mfma_f32_16x16x32_bf16 v[120:123], v[40:43], v[176:179], v[120:123]
	v_mfma_f32_16x16x32_bf16 v[116:119], v[64:67], v[176:179], v[116:119]
	v_mfma_f32_16x16x32_bf16 v[96:99], v[40:43], v[184:187], v[96:99]
	v_mfma_f32_16x16x32_bf16 v[92:95], v[64:67], v[184:187], v[92:95]
	v_mfma_f32_16x16x32_bf16 v[172:175], v[52:55], v[148:151], v[172:175]
	v_mfma_f32_16x16x32_bf16 v[168:171], v[76:79], v[148:151], v[168:171]
	v_mfma_f32_16x16x32_bf16 v[144:147], v[52:55], v[164:167], v[144:147]
	v_mfma_f32_16x16x32_bf16 v[140:143], v[76:79], v[164:167], v[140:143]
	v_mfma_f32_16x16x32_bf16 v[120:123], v[52:55], v[180:183], v[120:123]
	v_mfma_f32_16x16x32_bf16 v[116:119], v[76:79], v[180:183], v[116:119]
	v_mfma_f32_16x16x32_bf16 v[96:99], v[52:55], v[200:203], v[96:99]
	v_mfma_f32_16x16x32_bf16 v[92:95], v[76:79], v[200:203], v[92:95]
	s_setprio 0
	s_setprio 1
	v_mfma_f32_16x16x32_bf16 v[156:159], v[88:91], v[136:139], v[156:159]
	v_mfma_f32_16x16x32_bf16 v[132:135], v[88:91], v[160:163], v[132:135]
	v_mfma_f32_16x16x32_bf16 v[128:131], v[112:115], v[160:163], v[128:131]
	v_mfma_f32_16x16x32_bf16 v[108:111], v[88:91], v[176:179], v[108:111]
	v_mfma_f32_16x16x32_bf16 v[104:107], v[112:115], v[176:179], v[104:107]
	v_mfma_f32_16x16x32_bf16 v[84:87], v[88:91], v[184:187], v[84:87]
	v_mfma_f32_16x16x32_bf16 v[80:83], v[112:115], v[184:187], v[80:83]
	v_mfma_f32_16x16x32_bf16 v[156:159], v[100:103], v[148:151], v[156:159]
	v_mfma_f32_16x16x32_bf16 v[136:139], v[112:115], v[136:139], v[152:155]
	v_mfma_f32_16x16x32_bf16 v[132:135], v[100:103], v[164:167], v[132:135]
	v_mfma_f32_16x16x32_bf16 v[128:131], v[124:127], v[164:167], v[128:131]
	v_mfma_f32_16x16x32_bf16 v[108:111], v[100:103], v[180:183], v[108:111]
	v_mfma_f32_16x16x32_bf16 v[104:107], v[124:127], v[180:183], v[104:107]
	v_mfma_f32_16x16x32_bf16 v[84:87], v[100:103], v[200:203], v[84:87]
	v_mfma_f32_16x16x32_bf16 v[80:83], v[124:127], v[200:203], v[80:83]
	v_mfma_f32_16x16x32_bf16 v[136:139], v[124:127], v[148:151], v[136:139]
	s_setprio 0
	s_barrier
	s_add_i32 s80, s72, s63
	s_mov_b32 m0, s80
	ds_read_b128 v[148:151], v233 offset:16384
	ds_read_b128 v[152:155], v233 offset:17408
	ds_read_b128 v[160:163], v233 offset:18432
	ds_read_b128 v[164:167], v233 offset:19456
	ds_read_b128 v[176:179], v233 offset:20480
	ds_read_b128 v[180:183], v233 offset:21504
	ds_read_b128 v[184:187], v233 offset:22528
	ds_read_b128 v[200:203], v233 offset:23552
	global_load_lds_dwordx4 v190, s[48:49]
	s_add_i32 m0, s80, 0x2000
	s_add_u32 s80, s48, 0x40000
	s_addc_u32 s81, s49, 0
	s_add_i32 s90, s73, s63
	global_load_lds_dwordx4 v194, s[48:49]
	s_mov_b32 m0, s90
	s_nop 0
	global_load_lds_dwordx4 v190, s[80:81]
	s_add_i32 m0, s90, 0x2000
	s_nop 0
	global_load_lds_dwordx4 v194, s[80:81]
	s_mov_b32 m0, s64
	s_nop 0
	global_load_lds_dwordx4 v188, s[50:51]
	s_mov_b32 m0, s65
	s_nop 0
	global_load_lds_dwordx4 v192, s[50:51]
	s_waitcnt vmcnt(8)
	s_waitcnt lgkmcnt(0)
	s_barrier
	s_setprio 1
	s_waitcnt lgkmcnt(0)
	v_mfma_f32_16x16x32_bf16 v[72:75], v[40:43], v[148:151], v[72:75]
	v_mfma_f32_16x16x32_bf16 v[68:71], v[64:67], v[148:151], v[68:71]
	v_mfma_f32_16x16x32_bf16 v[48:51], v[40:43], v[160:163], v[48:51]
	v_mfma_f32_16x16x32_bf16 v[44:47], v[64:67], v[160:163], v[44:47]
	v_mfma_f32_16x16x32_bf16 v[28:31], v[40:43], v[176:179], v[28:31]
	v_mfma_f32_16x16x32_bf16 v[24:27], v[64:67], v[176:179], v[24:27]
	v_mfma_f32_16x16x32_bf16 v[12:15], v[40:43], v[184:187], v[12:15]
	v_mfma_f32_16x16x32_bf16 v[8:11], v[64:67], v[184:187], v[8:11]
	v_mfma_f32_16x16x32_bf16 v[72:75], v[52:55], v[152:155], v[72:75]
	v_mfma_f32_16x16x32_bf16 v[68:71], v[76:79], v[152:155], v[68:71]
	v_mfma_f32_16x16x32_bf16 v[48:51], v[52:55], v[164:167], v[48:51]
	v_mfma_f32_16x16x32_bf16 v[44:47], v[76:79], v[164:167], v[44:47]
	v_mfma_f32_16x16x32_bf16 v[28:31], v[52:55], v[180:183], v[28:31]
	v_mfma_f32_16x16x32_bf16 v[24:27], v[76:79], v[180:183], v[24:27]
	v_mfma_f32_16x16x32_bf16 v[12:15], v[52:55], v[200:203], v[12:15]
	v_mfma_f32_16x16x32_bf16 v[8:11], v[76:79], v[200:203], v[8:11]
	s_setprio 0
	s_setprio 1
	v_mfma_f32_16x16x32_bf16 v[36:39], v[88:91], v[160:163], v[36:39]
	v_mfma_f32_16x16x32_bf16 v[32:35], v[112:115], v[160:163], v[32:35]
	v_mfma_f32_16x16x32_bf16 v[20:23], v[88:91], v[176:179], v[20:23]
	v_mfma_f32_16x16x32_bf16 v[16:19], v[112:115], v[176:179], v[16:19]
	v_mfma_f32_16x16x32_bf16 v[4:7], v[88:91], v[184:187], v[4:7]
	v_mfma_f32_16x16x32_bf16 v[0:3], v[112:115], v[184:187], v[0:3]
	v_mfma_f32_16x16x32_bf16 v[40:43], v[88:91], v[148:151], v[60:63]
	v_mfma_f32_16x16x32_bf16 v[52:55], v[112:115], v[148:151], v[56:59]
	v_mfma_f32_16x16x32_bf16 v[36:39], v[100:103], v[164:167], v[36:39]
	v_mfma_f32_16x16x32_bf16 v[32:35], v[124:127], v[164:167], v[32:35]
	v_mfma_f32_16x16x32_bf16 v[20:23], v[100:103], v[180:183], v[20:23]
	v_mfma_f32_16x16x32_bf16 v[16:19], v[124:127], v[180:183], v[16:19]
	v_mfma_f32_16x16x32_bf16 v[4:7], v[100:103], v[200:203], v[4:7]
	v_mfma_f32_16x16x32_bf16 v[0:3], v[124:127], v[200:203], v[0:3]
	v_mfma_f32_16x16x32_bf16 v[40:43], v[100:103], v[152:155], v[40:43]
	v_mfma_f32_16x16x32_bf16 v[52:55], v[124:127], v[152:155], v[52:55]
	s_setprio 0
	s_barrier
	s_add_i32 s80, 0, 0x18000
	s_add_i32 s81, 0, 0x1c000
	v_add_u32_e32 v76, s80, v228
	v_add_u32_e32 v124, s81, v228
	ds_read_b128 v[56:59], v76
	ds_read_b128 v[60:63], v76 offset:1024
	ds_read_b128 v[64:67], v76 offset:2048
	ds_read_b128 v[76:79], v76 offset:3072
	ds_read_b128 v[88:91], v124
	ds_read_b128 v[100:103], v124 offset:1024
	ds_read_b128 v[112:115], v124 offset:2048
	ds_read_b128 v[124:127], v124 offset:3072
	s_add_u32 s100, s50, 0x80
	s_addc_u32 s101, s51, 0
	s_add_u32 s50, s50, 0x40000
	s_addc_u32 s51, s51, 0
	s_mov_b32 m0, s66
	ds_read_b128 v[148:151], v233 offset:32768
	ds_read_b128 v[152:155], v233 offset:33792
	ds_read_b128 v[160:163], v233 offset:34816
	ds_read_b128 v[164:167], v233 offset:35840
	ds_read_b128 v[176:179], v233 offset:36864
	ds_read_b128 v[180:183], v233 offset:37888
	ds_read_b128 v[184:187], v233 offset:38912
	ds_read_b128 v[200:203], v233 offset:39936
	global_load_lds_dwordx4 v188, s[50:51]
	s_mov_b32 m0, s67
	s_nop 0
	global_load_lds_dwordx4 v192, s[50:51]
	s_waitcnt vmcnt(8)
	s_waitcnt lgkmcnt(0)
	s_barrier
	s_setprio 1
	s_waitcnt lgkmcnt(0)
	v_mfma_f32_16x16x32_bf16 v[172:175], v[56:59], v[148:151], v[172:175]
	v_mfma_f32_16x16x32_bf16 v[168:171], v[64:67], v[148:151], v[168:171]
	v_mfma_f32_16x16x32_bf16 v[144:147], v[56:59], v[160:163], v[144:147]
	v_mfma_f32_16x16x32_bf16 v[140:143], v[64:67], v[160:163], v[140:143]
	v_mfma_f32_16x16x32_bf16 v[120:123], v[56:59], v[176:179], v[120:123]
	v_mfma_f32_16x16x32_bf16 v[116:119], v[64:67], v[176:179], v[116:119]
	v_mfma_f32_16x16x32_bf16 v[96:99], v[56:59], v[184:187], v[96:99]
	v_mfma_f32_16x16x32_bf16 v[92:95], v[64:67], v[184:187], v[92:95]
	v_mfma_f32_16x16x32_bf16 v[172:175], v[60:63], v[152:155], v[172:175]
	v_mfma_f32_16x16x32_bf16 v[168:171], v[76:79], v[152:155], v[168:171]
	v_mfma_f32_16x16x32_bf16 v[144:147], v[60:63], v[164:167], v[144:147]
	v_mfma_f32_16x16x32_bf16 v[140:143], v[76:79], v[164:167], v[140:143]
	v_mfma_f32_16x16x32_bf16 v[120:123], v[60:63], v[180:183], v[120:123]
	v_mfma_f32_16x16x32_bf16 v[116:119], v[76:79], v[180:183], v[116:119]
	v_mfma_f32_16x16x32_bf16 v[96:99], v[60:63], v[200:203], v[96:99]
	v_mfma_f32_16x16x32_bf16 v[92:95], v[76:79], v[200:203], v[92:95]
	s_setprio 0
	s_setprio 1
	v_mfma_f32_16x16x32_bf16 v[156:159], v[88:91], v[148:151], v[156:159]
	v_mfma_f32_16x16x32_bf16 v[136:139], v[112:115], v[148:151], v[136:139]
	v_mfma_f32_16x16x32_bf16 v[132:135], v[88:91], v[160:163], v[132:135]
	v_mfma_f32_16x16x32_bf16 v[128:131], v[112:115], v[160:163], v[128:131]
	v_mfma_f32_16x16x32_bf16 v[108:111], v[88:91], v[176:179], v[108:111]
	v_mfma_f32_16x16x32_bf16 v[104:107], v[112:115], v[176:179], v[104:107]
	v_mfma_f32_16x16x32_bf16 v[84:87], v[88:91], v[184:187], v[84:87]
	v_mfma_f32_16x16x32_bf16 v[80:83], v[112:115], v[184:187], v[80:83]
	v_mfma_f32_16x16x32_bf16 v[156:159], v[100:103], v[152:155], v[156:159]
	v_mfma_f32_16x16x32_bf16 v[152:155], v[124:127], v[152:155], v[136:139]
	v_mfma_f32_16x16x32_bf16 v[132:135], v[100:103], v[164:167], v[132:135]
	v_mfma_f32_16x16x32_bf16 v[128:131], v[124:127], v[164:167], v[128:131]
	v_mfma_f32_16x16x32_bf16 v[108:111], v[100:103], v[180:183], v[108:111]
	v_mfma_f32_16x16x32_bf16 v[104:107], v[124:127], v[180:183], v[104:107]
	v_mfma_f32_16x16x32_bf16 v[84:87], v[100:103], v[200:203], v[84:87]
	v_mfma_f32_16x16x32_bf16 v[80:83], v[124:127], v[200:203], v[80:83]
	s_setprio 0
	s_barrier
	s_add_i32 s50, s80, s63
	s_mov_b32 m0, s50
	ds_read_b128 v[136:139], v233 offset:49152
	ds_read_b128 v[148:151], v233 offset:50176
	ds_read_b128 v[160:163], v233 offset:51200
	ds_read_b128 v[164:167], v233 offset:52224
	ds_read_b128 v[176:179], v233 offset:53248
	ds_read_b128 v[180:183], v233 offset:54272
	ds_read_b128 v[184:187], v233 offset:55296
	ds_read_b128 v[200:203], v233 offset:56320
	s_add_u32 s98, s48, 0x80
	s_addc_u32 s99, s49, 0
	global_load_lds_dwordx4 v190, s[98:99]
	s_add_i32 m0, s50, 0x2000
	s_add_u32 s48, s48, 0x40080
	s_addc_u32 s49, s49, 0
	s_add_i32 s50, s81, s63
	global_load_lds_dwordx4 v194, s[98:99]
	s_mov_b32 m0, s50
	s_nop 0
	global_load_lds_dwordx4 v190, s[48:49]
	s_add_i32 m0, s50, 0x2000
	s_nop 0
	global_load_lds_dwordx4 v194, s[48:49]
	s_mov_b32 m0, s69
	s_nop 0
	global_load_lds_dwordx4 v188, s[100:101]
	s_mov_b32 m0, s70
	s_nop 0
	global_load_lds_dwordx4 v192, s[100:101]
	s_waitcnt vmcnt(8)
	s_waitcnt lgkmcnt(0)
	s_barrier
	s_setprio 1
	s_waitcnt lgkmcnt(0)
	v_mfma_f32_16x16x32_bf16 v[72:75], v[56:59], v[136:139], v[72:75]
	v_mfma_f32_16x16x32_bf16 v[68:71], v[64:67], v[136:139], v[68:71]
	v_mfma_f32_16x16x32_bf16 v[48:51], v[56:59], v[160:163], v[48:51]
	v_mfma_f32_16x16x32_bf16 v[44:47], v[64:67], v[160:163], v[44:47]
	v_mfma_f32_16x16x32_bf16 v[28:31], v[56:59], v[176:179], v[28:31]
	v_mfma_f32_16x16x32_bf16 v[24:27], v[64:67], v[176:179], v[24:27]
	v_mfma_f32_16x16x32_bf16 v[12:15], v[56:59], v[184:187], v[12:15]
	v_mfma_f32_16x16x32_bf16 v[8:11], v[64:67], v[184:187], v[8:11]
	v_mfma_f32_16x16x32_bf16 v[72:75], v[60:63], v[148:151], v[72:75]
	v_mfma_f32_16x16x32_bf16 v[68:71], v[76:79], v[148:151], v[68:71]
	v_mfma_f32_16x16x32_bf16 v[48:51], v[60:63], v[164:167], v[48:51]
	v_mfma_f32_16x16x32_bf16 v[44:47], v[76:79], v[164:167], v[44:47]
	v_mfma_f32_16x16x32_bf16 v[28:31], v[60:63], v[180:183], v[28:31]
	v_mfma_f32_16x16x32_bf16 v[24:27], v[76:79], v[180:183], v[24:27]
	v_mfma_f32_16x16x32_bf16 v[12:15], v[60:63], v[200:203], v[12:15]
	v_mfma_f32_16x16x32_bf16 v[8:11], v[76:79], v[200:203], v[8:11]
	s_setprio 0
	s_setprio 1
	v_mfma_f32_16x16x32_bf16 v[40:43], v[88:91], v[136:139], v[40:43]
	v_mfma_f32_16x16x32_bf16 v[60:63], v[100:103], v[148:151], v[40:43]
	v_mfma_f32_16x16x32_bf16 v[40:43], v[112:115], v[136:139], v[52:55]
	v_mfma_f32_16x16x32_bf16 v[36:39], v[88:91], v[160:163], v[36:39]
	v_mfma_f32_16x16x32_bf16 v[32:35], v[112:115], v[160:163], v[32:35]
	v_mfma_f32_16x16x32_bf16 v[20:23], v[88:91], v[176:179], v[20:23]
	v_mfma_f32_16x16x32_bf16 v[16:19], v[112:115], v[176:179], v[16:19]
	v_mfma_f32_16x16x32_bf16 v[4:7], v[88:91], v[184:187], v[4:7]
	v_mfma_f32_16x16x32_bf16 v[0:3], v[112:115], v[184:187], v[0:3]
	v_mfma_f32_16x16x32_bf16 v[56:59], v[124:127], v[148:151], v[40:43]
	v_mfma_f32_16x16x32_bf16 v[36:39], v[100:103], v[164:167], v[36:39]
	v_mfma_f32_16x16x32_bf16 v[32:35], v[124:127], v[164:167], v[32:35]
	v_mfma_f32_16x16x32_bf16 v[20:23], v[100:103], v[180:183], v[20:23]
	v_mfma_f32_16x16x32_bf16 v[16:19], v[124:127], v[180:183], v[16:19]
	v_mfma_f32_16x16x32_bf16 v[4:7], v[100:103], v[200:203], v[4:7]
	v_mfma_f32_16x16x32_bf16 v[0:3], v[124:127], v[200:203], v[0:3]
	s_setprio 0
	s_barrier
	s_add_i32 s79, s79, 2
	s_add_u32 s53, s53, 0x100
	s_addc_u32 s78, s78, 0
	s_add_u32 s46, s46, 0x100
	s_addc_u32 s47, s47, 0
	s_cmp_gt_u32 s79, 13
	s_cbranch_scc0 .LBB0_811
	s_and_b64 vcc, exec, s[28:29]
	s_cbranch_vccz .LBB0_814
	s_barrier

.LBB0_1835:
	ds_read_b128 v[130:133], v165
	ds_read_b128 v[134:137], v165 offset:1024
	ds_read_b128 v[138:141], v165 offset:2048
	ds_read_b128 v[158:161], v165 offset:3072
	ds_read_b128 v[170:173], v166
	ds_read_b128 v[174:177], v166 offset:1024
	ds_read_b128 v[178:181], v166 offset:2048
	ds_read_b128 v[182:185], v166 offset:3072
	s_add_u32 s46, s44, 0xfffc0080
	s_addc_u32 s47, s45, -1
	s_cmp_eq_u32 s37, 12
	s_cselect_b32 s49, s39, s47
	s_cselect_b32 s48, s38, s46
	s_cselect_b32 s47, s41, s35
	s_cselect_b32 s46, s40, s5
	s_add_i32 m0, s43, 0xc000
	ds_read_b128 v[186:189], v167
	ds_read_b128 v[190:193], v167 offset:1024
	ds_read_b128 v[194:197], v167 offset:2048
	ds_read_b128 v[198:201], v167 offset:3072
	ds_read_b128 v[202:205], v167 offset:4096
	ds_read_b128 v[206:209], v167 offset:5120
	ds_read_b128 v[210:213], v167 offset:6144
	ds_read_b128 v[214:217], v167 offset:7168
	global_load_lds_dwordx4 v154, s[44:45]
	s_add_i32 m0, s43, 0xe000
	s_nop 0
	global_load_lds_dwordx4 v152, s[44:45]
	s_waitcnt vmcnt(8)
	s_waitcnt lgkmcnt(0)
	s_barrier
	s_setprio 1
	s_waitcnt lgkmcnt(0)
	v_mfma_f32_16x16x32_bf16 v[124:127], v[130:133], v[186:189], v[124:127]
	v_mfma_f32_16x16x32_bf16 v[120:123], v[138:141], v[186:189], v[120:123]
	v_mfma_f32_16x16x32_bf16 v[112:115], v[130:133], v[194:197], v[112:115]
	v_mfma_f32_16x16x32_bf16 v[104:107], v[138:141], v[194:197], v[104:107]
	v_mfma_f32_16x16x32_bf16 v[96:99], v[130:133], v[202:205], v[96:99]
	v_mfma_f32_16x16x32_bf16 v[88:91], v[138:141], v[202:205], v[88:91]
	v_mfma_f32_16x16x32_bf16 v[80:83], v[130:133], v[210:213], v[80:83]
	v_mfma_f32_16x16x32_bf16 v[72:75], v[138:141], v[210:213], v[72:75]
	v_mfma_f32_16x16x32_bf16 v[124:127], v[134:137], v[190:193], v[124:127]
	v_mfma_f32_16x16x32_bf16 v[120:123], v[158:161], v[190:193], v[120:123]
	v_mfma_f32_16x16x32_bf16 v[112:115], v[134:137], v[198:201], v[112:115]
	v_mfma_f32_16x16x32_bf16 v[104:107], v[158:161], v[198:201], v[104:107]
	v_mfma_f32_16x16x32_bf16 v[96:99], v[134:137], v[206:209], v[96:99]
	v_mfma_f32_16x16x32_bf16 v[88:91], v[158:161], v[206:209], v[88:91]
	v_mfma_f32_16x16x32_bf16 v[80:83], v[134:137], v[214:217], v[80:83]
	v_mfma_f32_16x16x32_bf16 v[72:75], v[158:161], v[214:217], v[72:75]
	s_setprio 0
	s_setprio 1
	v_mfma_f32_16x16x32_bf16 v[116:119], v[170:173], v[186:189], v[116:119]
	v_mfma_f32_16x16x32_bf16 v[108:111], v[178:181], v[186:189], v[108:111]
	v_mfma_f32_16x16x32_bf16 v[100:103], v[170:173], v[194:197], v[100:103]
	v_mfma_f32_16x16x32_bf16 v[92:95], v[178:181], v[194:197], v[92:95]
	v_mfma_f32_16x16x32_bf16 v[84:87], v[170:173], v[202:205], v[84:87]
	v_mfma_f32_16x16x32_bf16 v[76:79], v[178:181], v[202:205], v[76:79]
	v_mfma_f32_16x16x32_bf16 v[68:71], v[170:173], v[210:213], v[68:71]
	v_mfma_f32_16x16x32_bf16 v[64:67], v[178:181], v[210:213], v[64:67]
	v_mfma_f32_16x16x32_bf16 v[116:119], v[174:177], v[190:193], v[116:119]
	v_mfma_f32_16x16x32_bf16 v[108:111], v[182:185], v[190:193], v[108:111]
	v_mfma_f32_16x16x32_bf16 v[100:103], v[174:177], v[198:201], v[100:103]
	v_mfma_f32_16x16x32_bf16 v[92:95], v[182:185], v[198:201], v[92:95]
	v_mfma_f32_16x16x32_bf16 v[84:87], v[174:177], v[206:209], v[84:87]
	v_mfma_f32_16x16x32_bf16 v[76:79], v[182:185], v[206:209], v[76:79]
	v_mfma_f32_16x16x32_bf16 v[68:71], v[174:177], v[214:217], v[68:71]
	v_mfma_f32_16x16x32_bf16 v[64:67], v[182:185], v[214:217], v[64:67]
	s_setprio 0
	s_barrier
	s_add_i32 s73, s67, s58
	s_mov_b32 m0, s73
	ds_read_b128 v[186:189], v167 offset:16384
	ds_read_b128 v[190:193], v167 offset:17408
	ds_read_b128 v[194:197], v167 offset:18432
	ds_read_b128 v[198:201], v167 offset:19456
	ds_read_b128 v[202:205], v167 offset:20480
	ds_read_b128 v[206:209], v167 offset:21504
	ds_read_b128 v[210:213], v167 offset:22528
	ds_read_b128 v[214:217], v167 offset:23552
	global_load_lds_dwordx4 v144, s[46:47]
	s_add_i32 m0, s73, 0x2000
	s_add_u32 s74, s46, 0x40000
	s_addc_u32 s75, s47, 0
	s_add_i32 s73, s68, s58
	global_load_lds_dwordx4 v150, s[46:47]
	s_mov_b32 m0, s73
	s_nop 0
	global_load_lds_dwordx4 v144, s[74:75]
	s_add_i32 m0, s73, 0x2000
	s_nop 0
	global_load_lds_dwordx4 v150, s[74:75]
	s_mov_b32 m0, s43
	s_nop 0
	global_load_lds_dwordx4 v146, s[48:49]
	s_mov_b32 m0, s59
	s_nop 0
	global_load_lds_dwordx4 v148, s[48:49]
	s_waitcnt vmcnt(8)
	s_waitcnt lgkmcnt(0)
	s_barrier
	s_setprio 1
	s_waitcnt lgkmcnt(0)
	v_mfma_f32_16x16x32_bf16 v[60:63], v[130:133], v[186:189], v[60:63]
	v_mfma_f32_16x16x32_bf16 v[56:59], v[138:141], v[186:189], v[56:59]
	v_mfma_f32_16x16x32_bf16 v[48:51], v[130:133], v[194:197], v[48:51]
	v_mfma_f32_16x16x32_bf16 v[40:43], v[138:141], v[194:197], v[40:43]
	v_mfma_f32_16x16x32_bf16 v[32:35], v[130:133], v[202:205], v[32:35]
	v_mfma_f32_16x16x32_bf16 v[24:27], v[138:141], v[202:205], v[24:27]
	v_mfma_f32_16x16x32_bf16 v[16:19], v[130:133], v[210:213], v[16:19]
	v_mfma_f32_16x16x32_bf16 v[8:11], v[138:141], v[210:213], v[8:11]
	v_mfma_f32_16x16x32_bf16 v[60:63], v[134:137], v[190:193], v[60:63]
	v_mfma_f32_16x16x32_bf16 v[56:59], v[158:161], v[190:193], v[56:59]
	v_mfma_f32_16x16x32_bf16 v[48:51], v[134:137], v[198:201], v[48:51]
	v_mfma_f32_16x16x32_bf16 v[40:43], v[158:161], v[198:201], v[40:43]
	v_mfma_f32_16x16x32_bf16 v[32:35], v[134:137], v[206:209], v[32:35]
	v_mfma_f32_16x16x32_bf16 v[24:27], v[158:161], v[206:209], v[24:27]
	v_mfma_f32_16x16x32_bf16 v[16:19], v[134:137], v[214:217], v[16:19]
	v_mfma_f32_16x16x32_bf16 v[8:11], v[158:161], v[214:217], v[8:11]
	s_setprio 0
	s_setprio 1
	v_mfma_f32_16x16x32_bf16 v[52:55], v[170:173], v[186:189], v[52:55]
	v_mfma_f32_16x16x32_bf16 v[44:47], v[178:181], v[186:189], v[44:47]
	v_mfma_f32_16x16x32_bf16 v[36:39], v[170:173], v[194:197], v[36:39]
	v_mfma_f32_16x16x32_bf16 v[28:31], v[178:181], v[194:197], v[28:31]
	v_mfma_f32_16x16x32_bf16 v[20:23], v[170:173], v[202:205], v[20:23]
	v_mfma_f32_16x16x32_bf16 v[12:15], v[178:181], v[202:205], v[12:15]
	v_mfma_f32_16x16x32_bf16 v[4:7], v[170:173], v[210:213], v[4:7]
	v_mfma_f32_16x16x32_bf16 v[0:3], v[178:181], v[210:213], v[0:3]
	v_mfma_f32_16x16x32_bf16 v[52:55], v[174:177], v[190:193], v[52:55]
	v_mfma_f32_16x16x32_bf16 v[44:47], v[182:185], v[190:193], v[44:47]
	v_mfma_f32_16x16x32_bf16 v[36:39], v[174:177], v[198:201], v[36:39]
	v_mfma_f32_16x16x32_bf16 v[28:31], v[182:185], v[198:201], v[28:31]
	v_mfma_f32_16x16x32_bf16 v[20:23], v[174:177], v[206:209], v[20:23]
	v_mfma_f32_16x16x32_bf16 v[12:15], v[182:185], v[206:209], v[12:15]
	v_mfma_f32_16x16x32_bf16 v[4:7], v[174:177], v[214:217], v[4:7]
	v_mfma_f32_16x16x32_bf16 v[0:3], v[182:185], v[214:217], v[0:3]
	s_setprio 0
	s_barrier
	s_add_i32 s73, 0, 0x18000
	v_add_u32_e32 v129, s73, v162
	s_add_i32 s74, 0, 0x1c000
	ds_read_b128 v[130:133], v129
	ds_read_b128 v[134:137], v129 offset:1024
	ds_read_b128 v[138:141], v129 offset:2048
	ds_read_b128 v[158:161], v129 offset:3072
	v_add_u32_e32 v129, s74, v162
	ds_read_b128 v[170:173], v129
	ds_read_b128 v[174:177], v129 offset:1024
	ds_read_b128 v[178:181], v129 offset:2048
	ds_read_b128 v[182:185], v129 offset:3072
	s_add_u32 s100, s48, 0x80
	s_addc_u32 s101, s49, 0
	s_add_u32 s48, s48, 0x40000
	s_addc_u32 s49, s49, 0
	s_mov_b32 m0, s60
	ds_read_b128 v[186:189], v167 offset:32768
	ds_read_b128 v[190:193], v167 offset:33792
	ds_read_b128 v[194:197], v167 offset:34816
	ds_read_b128 v[198:201], v167 offset:35840
	ds_read_b128 v[202:205], v167 offset:36864
	ds_read_b128 v[206:209], v167 offset:37888
	ds_read_b128 v[210:213], v167 offset:38912
	ds_read_b128 v[214:217], v167 offset:39936
	global_load_lds_dwordx4 v146, s[48:49]
	s_mov_b32 m0, s61
	s_nop 0
	global_load_lds_dwordx4 v148, s[48:49]
	s_waitcnt vmcnt(8)
	s_waitcnt lgkmcnt(0)
	s_barrier
	s_setprio 1
	s_waitcnt lgkmcnt(0)
	v_mfma_f32_16x16x32_bf16 v[124:127], v[130:133], v[186:189], v[124:127]
	v_mfma_f32_16x16x32_bf16 v[120:123], v[138:141], v[186:189], v[120:123]
	v_mfma_f32_16x16x32_bf16 v[112:115], v[130:133], v[194:197], v[112:115]
	v_mfma_f32_16x16x32_bf16 v[104:107], v[138:141], v[194:197], v[104:107]
	v_mfma_f32_16x16x32_bf16 v[96:99], v[130:133], v[202:205], v[96:99]
	v_mfma_f32_16x16x32_bf16 v[88:91], v[138:141], v[202:205], v[88:91]
	v_mfma_f32_16x16x32_bf16 v[80:83], v[130:133], v[210:213], v[80:83]
	v_mfma_f32_16x16x32_bf16 v[72:75], v[138:141], v[210:213], v[72:75]
	v_mfma_f32_16x16x32_bf16 v[124:127], v[134:137], v[190:193], v[124:127]
	v_mfma_f32_16x16x32_bf16 v[120:123], v[158:161], v[190:193], v[120:123]
	v_mfma_f32_16x16x32_bf16 v[112:115], v[134:137], v[198:201], v[112:115]
	v_mfma_f32_16x16x32_bf16 v[104:107], v[158:161], v[198:201], v[104:107]
	v_mfma_f32_16x16x32_bf16 v[96:99], v[134:137], v[206:209], v[96:99]
	v_mfma_f32_16x16x32_bf16 v[88:91], v[158:161], v[206:209], v[88:91]
	v_mfma_f32_16x16x32_bf16 v[80:83], v[134:137], v[214:217], v[80:83]
	v_mfma_f32_16x16x32_bf16 v[72:75], v[158:161], v[214:217], v[72:75]
	s_setprio 0
	s_setprio 1
	v_mfma_f32_16x16x32_bf16 v[116:119], v[170:173], v[186:189], v[116:119]
	v_mfma_f32_16x16x32_bf16 v[108:111], v[178:181], v[186:189], v[108:111]
	v_mfma_f32_16x16x32_bf16 v[100:103], v[170:173], v[194:197], v[100:103]
	v_mfma_f32_16x16x32_bf16 v[92:95], v[178:181], v[194:197], v[92:95]
	v_mfma_f32_16x16x32_bf16 v[84:87], v[170:173], v[202:205], v[84:87]
	v_mfma_f32_16x16x32_bf16 v[76:79], v[178:181], v[202:205], v[76:79]
	v_mfma_f32_16x16x32_bf16 v[68:71], v[170:173], v[210:213], v[68:71]
	v_mfma_f32_16x16x32_bf16 v[64:67], v[178:181], v[210:213], v[64:67]
	v_mfma_f32_16x16x32_bf16 v[116:119], v[174:177], v[190:193], v[116:119]
	v_mfma_f32_16x16x32_bf16 v[108:111], v[182:185], v[190:193], v[108:111]
	v_mfma_f32_16x16x32_bf16 v[100:103], v[174:177], v[198:201], v[100:103]
	v_mfma_f32_16x16x32_bf16 v[92:95], v[182:185], v[198:201], v[92:95]
	v_mfma_f32_16x16x32_bf16 v[84:87], v[174:177], v[206:209], v[84:87]
	v_mfma_f32_16x16x32_bf16 v[76:79], v[182:185], v[206:209], v[76:79]
	v_mfma_f32_16x16x32_bf16 v[68:71], v[174:177], v[214:217], v[68:71]
	v_mfma_f32_16x16x32_bf16 v[64:67], v[182:185], v[214:217], v[64:67]
	s_setprio 0
	s_barrier
	s_add_i32 s48, s73, s58
	s_mov_b32 m0, s48
	ds_read_b128 v[186:189], v167 offset:49152
	ds_read_b128 v[190:193], v167 offset:50176
	ds_read_b128 v[194:197], v167 offset:51200
	ds_read_b128 v[198:201], v167 offset:52224
	ds_read_b128 v[202:205], v167 offset:53248
	ds_read_b128 v[206:209], v167 offset:54272
	ds_read_b128 v[210:213], v167 offset:55296
	ds_read_b128 v[214:217], v167 offset:56320
	s_add_u32 s98, s46, 0x80
	s_addc_u32 s99, s47, 0
	global_load_lds_dwordx4 v144, s[98:99]
	s_add_i32 m0, s48, 0x2000
	s_add_u32 s46, s46, 0x40080
	s_addc_u32 s47, s47, 0
	s_add_i32 s48, s74, s58
	global_load_lds_dwordx4 v150, s[98:99]
	s_mov_b32 m0, s48
	s_nop 0
	global_load_lds_dwordx4 v144, s[46:47]
	s_add_i32 m0, s48, 0x2000
	s_nop 0
	global_load_lds_dwordx4 v150, s[46:47]
	s_mov_b32 m0, s64
	s_nop 0
	global_load_lds_dwordx4 v146, s[100:101]
	s_mov_b32 m0, s65
	s_nop 0
	global_load_lds_dwordx4 v148, s[100:101]
	s_waitcnt vmcnt(8)
	s_waitcnt lgkmcnt(0)
	s_barrier
	s_setprio 1
	s_waitcnt lgkmcnt(0)
	v_mfma_f32_16x16x32_bf16 v[60:63], v[130:133], v[186:189], v[60:63]
	v_mfma_f32_16x16x32_bf16 v[56:59], v[138:141], v[186:189], v[56:59]
	v_mfma_f32_16x16x32_bf16 v[48:51], v[130:133], v[194:197], v[48:51]
	v_mfma_f32_16x16x32_bf16 v[40:43], v[138:141], v[194:197], v[40:43]
	v_mfma_f32_16x16x32_bf16 v[32:35], v[130:133], v[202:205], v[32:35]
	v_mfma_f32_16x16x32_bf16 v[24:27], v[138:141], v[202:205], v[24:27]
	v_mfma_f32_16x16x32_bf16 v[16:19], v[130:133], v[210:213], v[16:19]
	v_mfma_f32_16x16x32_bf16 v[8:11], v[138:141], v[210:213], v[8:11]
	v_mfma_f32_16x16x32_bf16 v[60:63], v[134:137], v[190:193], v[60:63]
	v_mfma_f32_16x16x32_bf16 v[56:59], v[158:161], v[190:193], v[56:59]
	v_mfma_f32_16x16x32_bf16 v[48:51], v[134:137], v[198:201], v[48:51]
	v_mfma_f32_16x16x32_bf16 v[40:43], v[158:161], v[198:201], v[40:43]
	v_mfma_f32_16x16x32_bf16 v[32:35], v[134:137], v[206:209], v[32:35]
	v_mfma_f32_16x16x32_bf16 v[24:27], v[158:161], v[206:209], v[24:27]
	v_mfma_f32_16x16x32_bf16 v[16:19], v[134:137], v[214:217], v[16:19]
	v_mfma_f32_16x16x32_bf16 v[8:11], v[158:161], v[214:217], v[8:11]
	s_setprio 0
	s_setprio 1
	v_mfma_f32_16x16x32_bf16 v[52:55], v[170:173], v[186:189], v[52:55]
	v_mfma_f32_16x16x32_bf16 v[44:47], v[178:181], v[186:189], v[44:47]
	v_mfma_f32_16x16x32_bf16 v[36:39], v[170:173], v[194:197], v[36:39]
	v_mfma_f32_16x16x32_bf16 v[28:31], v[178:181], v[194:197], v[28:31]
	v_mfma_f32_16x16x32_bf16 v[20:23], v[170:173], v[202:205], v[20:23]
	v_mfma_f32_16x16x32_bf16 v[12:15], v[178:181], v[202:205], v[12:15]
	v_mfma_f32_16x16x32_bf16 v[4:7], v[170:173], v[210:213], v[4:7]
	v_mfma_f32_16x16x32_bf16 v[0:3], v[178:181], v[210:213], v[0:3]
	v_mfma_f32_16x16x32_bf16 v[52:55], v[174:177], v[190:193], v[52:55]
	v_mfma_f32_16x16x32_bf16 v[44:47], v[182:185], v[190:193], v[44:47]
	v_mfma_f32_16x16x32_bf16 v[36:39], v[174:177], v[198:201], v[36:39]
	v_mfma_f32_16x16x32_bf16 v[28:31], v[182:185], v[198:201], v[28:31]
	v_mfma_f32_16x16x32_bf16 v[20:23], v[174:177], v[206:209], v[20:23]
	v_mfma_f32_16x16x32_bf16 v[12:15], v[182:185], v[206:209], v[12:15]
	v_mfma_f32_16x16x32_bf16 v[4:7], v[174:177], v[214:217], v[4:7]
	v_mfma_f32_16x16x32_bf16 v[0:3], v[182:185], v[214:217], v[0:3]
	s_setprio 0
	s_barrier
	s_add_i32 s37, s37, 2
	s_add_u32 s5, s5, 0x100
	s_addc_u32 s35, s35, 0
	s_add_u32 s44, s44, 0x100
	s_addc_u32 s45, s45, 0
	s_cmp_gt_u32 s37, 13
	s_cbranch_scc0 .LBB0_1835
	s_and_b64 vcc, exec, s[22:23]
	s_cbranch_vccz .LBB0_1838
	s_barrier

.LBB0_3651:
	ds_read_b128 v[130:133], v163
	ds_read_b128 v[134:137], v163 offset:1024
	ds_read_b128 v[138:141], v163 offset:2048
	ds_read_b128 v[168:171], v163 offset:3072
	ds_read_b128 v[172:175], v164
	ds_read_b128 v[176:179], v164 offset:1024
	ds_read_b128 v[180:183], v164 offset:2048
	ds_read_b128 v[184:187], v164 offset:3072
	s_add_u32 s44, s42, 0xfffc0080
	s_addc_u32 s45, s43, -1
	s_cmp_eq_u32 s70, 12
	s_cselect_b32 s47, s35, s45
	s_cselect_b32 s46, s34, s44
	s_cselect_b32 s45, s37, s31
	s_cselect_b32 s44, s36, s29
	s_add_i32 m0, s39, 0xc000
	ds_read_b128 v[188:191], v165
	ds_read_b128 v[192:195], v165 offset:1024
	ds_read_b128 v[196:199], v165 offset:2048
	ds_read_b128 v[200:203], v165 offset:3072
	ds_read_b128 v[204:207], v165 offset:4096
	ds_read_b128 v[208:211], v165 offset:5120
	ds_read_b128 v[212:215], v165 offset:6144
	ds_read_b128 v[216:219], v165 offset:7168
	global_load_lds_dwordx4 v154, s[42:43]
	s_add_i32 m0, s39, 0xe000
	s_nop 0
	global_load_lds_dwordx4 v152, s[42:43]
	s_waitcnt vmcnt(8)
	s_waitcnt lgkmcnt(0)
	s_barrier
	s_setprio 1
	s_waitcnt lgkmcnt(0)
	v_mfma_f32_16x16x32_bf16 v[124:127], v[130:133], v[188:191], v[124:127]
	v_mfma_f32_16x16x32_bf16 v[120:123], v[138:141], v[188:191], v[120:123]
	v_mfma_f32_16x16x32_bf16 v[116:119], v[130:133], v[196:199], v[116:119]
	v_mfma_f32_16x16x32_bf16 v[112:115], v[138:141], v[196:199], v[112:115]
	v_mfma_f32_16x16x32_bf16 v[108:111], v[130:133], v[204:207], v[108:111]
	v_mfma_f32_16x16x32_bf16 v[100:103], v[138:141], v[204:207], v[100:103]
	v_mfma_f32_16x16x32_bf16 v[92:95], v[130:133], v[212:215], v[92:95]
	v_mfma_f32_16x16x32_bf16 v[84:87], v[138:141], v[212:215], v[84:87]
	v_mfma_f32_16x16x32_bf16 v[124:127], v[134:137], v[192:195], v[124:127]
	v_mfma_f32_16x16x32_bf16 v[120:123], v[168:171], v[192:195], v[120:123]
	v_mfma_f32_16x16x32_bf16 v[116:119], v[134:137], v[200:203], v[116:119]
	v_mfma_f32_16x16x32_bf16 v[112:115], v[168:171], v[200:203], v[112:115]
	v_mfma_f32_16x16x32_bf16 v[108:111], v[134:137], v[208:211], v[108:111]
	v_mfma_f32_16x16x32_bf16 v[100:103], v[168:171], v[208:211], v[100:103]
	v_mfma_f32_16x16x32_bf16 v[92:95], v[134:137], v[216:219], v[92:95]
	v_mfma_f32_16x16x32_bf16 v[84:87], v[168:171], v[216:219], v[84:87]
	s_setprio 0
	s_setprio 1
	v_mfma_f32_16x16x32_bf16 v[104:107], v[172:175], v[188:191], v[104:107]
	v_mfma_f32_16x16x32_bf16 v[96:99], v[180:183], v[188:191], v[96:99]
	v_mfma_f32_16x16x32_bf16 v[88:91], v[172:175], v[196:199], v[88:91]
	v_mfma_f32_16x16x32_bf16 v[80:83], v[180:183], v[196:199], v[80:83]
	v_mfma_f32_16x16x32_bf16 v[76:79], v[172:175], v[204:207], v[76:79]
	v_mfma_f32_16x16x32_bf16 v[72:75], v[180:183], v[204:207], v[72:75]
	v_mfma_f32_16x16x32_bf16 v[68:71], v[172:175], v[212:215], v[68:71]
	v_mfma_f32_16x16x32_bf16 v[64:67], v[180:183], v[212:215], v[64:67]
	v_mfma_f32_16x16x32_bf16 v[104:107], v[176:179], v[192:195], v[104:107]
	v_mfma_f32_16x16x32_bf16 v[96:99], v[184:187], v[192:195], v[96:99]
	v_mfma_f32_16x16x32_bf16 v[88:91], v[176:179], v[200:203], v[88:91]
	v_mfma_f32_16x16x32_bf16 v[80:83], v[184:187], v[200:203], v[80:83]
	v_mfma_f32_16x16x32_bf16 v[76:79], v[176:179], v[208:211], v[76:79]
	v_mfma_f32_16x16x32_bf16 v[72:75], v[184:187], v[208:211], v[72:75]
	v_mfma_f32_16x16x32_bf16 v[68:71], v[176:179], v[216:219], v[68:71]
	v_mfma_f32_16x16x32_bf16 v[64:67], v[184:187], v[216:219], v[64:67]
	s_setprio 0
	s_barrier
	s_add_i32 s71, s64, s56
	s_mov_b32 m0, s71
	ds_read_b128 v[188:191], v165 offset:16384
	ds_read_b128 v[192:195], v165 offset:17408
	ds_read_b128 v[196:199], v165 offset:18432
	ds_read_b128 v[200:203], v165 offset:19456
	ds_read_b128 v[204:207], v165 offset:20480
	ds_read_b128 v[208:211], v165 offset:21504
	ds_read_b128 v[212:215], v165 offset:22528
	ds_read_b128 v[216:219], v165 offset:23552
	global_load_lds_dwordx4 v144, s[44:45]
	s_add_i32 m0, s71, 0x2000
	s_add_u32 s72, s44, 0x40000
	s_addc_u32 s73, s45, 0
	s_add_i32 s71, s65, s56
	global_load_lds_dwordx4 v150, s[44:45]
	s_mov_b32 m0, s71
	s_nop 0
	global_load_lds_dwordx4 v144, s[72:73]
	s_add_i32 m0, s71, 0x2000
	s_nop 0
	global_load_lds_dwordx4 v150, s[72:73]
	s_mov_b32 m0, s39
	s_nop 0
	global_load_lds_dwordx4 v146, s[46:47]
	s_mov_b32 m0, s41
	s_nop 0
	global_load_lds_dwordx4 v148, s[46:47]
	s_waitcnt vmcnt(8)
	s_waitcnt lgkmcnt(0)
	s_barrier
	s_setprio 1
	s_waitcnt lgkmcnt(0)
	v_mfma_f32_16x16x32_bf16 v[60:63], v[130:133], v[188:191], v[60:63]
	v_mfma_f32_16x16x32_bf16 v[56:59], v[138:141], v[188:191], v[56:59]
	v_mfma_f32_16x16x32_bf16 v[48:51], v[130:133], v[196:199], v[48:51]
	v_mfma_f32_16x16x32_bf16 v[40:43], v[138:141], v[196:199], v[40:43]
	v_mfma_f32_16x16x32_bf16 v[32:35], v[130:133], v[204:207], v[32:35]
	v_mfma_f32_16x16x32_bf16 v[24:27], v[138:141], v[204:207], v[24:27]
	v_mfma_f32_16x16x32_bf16 v[16:19], v[130:133], v[212:215], v[16:19]
	v_mfma_f32_16x16x32_bf16 v[8:11], v[138:141], v[212:215], v[8:11]
	v_mfma_f32_16x16x32_bf16 v[60:63], v[134:137], v[192:195], v[60:63]
	v_mfma_f32_16x16x32_bf16 v[56:59], v[168:171], v[192:195], v[56:59]
	v_mfma_f32_16x16x32_bf16 v[48:51], v[134:137], v[200:203], v[48:51]
	v_mfma_f32_16x16x32_bf16 v[40:43], v[168:171], v[200:203], v[40:43]
	v_mfma_f32_16x16x32_bf16 v[32:35], v[134:137], v[208:211], v[32:35]
	v_mfma_f32_16x16x32_bf16 v[24:27], v[168:171], v[208:211], v[24:27]
	v_mfma_f32_16x16x32_bf16 v[16:19], v[134:137], v[216:219], v[16:19]
	v_mfma_f32_16x16x32_bf16 v[8:11], v[168:171], v[216:219], v[8:11]
	s_setprio 0
	s_setprio 1
	v_mfma_f32_16x16x32_bf16 v[52:55], v[172:175], v[188:191], v[52:55]
	v_mfma_f32_16x16x32_bf16 v[44:47], v[180:183], v[188:191], v[44:47]
	v_mfma_f32_16x16x32_bf16 v[36:39], v[172:175], v[196:199], v[36:39]
	v_mfma_f32_16x16x32_bf16 v[28:31], v[180:183], v[196:199], v[28:31]
	v_mfma_f32_16x16x32_bf16 v[20:23], v[172:175], v[204:207], v[20:23]
	v_mfma_f32_16x16x32_bf16 v[12:15], v[180:183], v[204:207], v[12:15]
	v_mfma_f32_16x16x32_bf16 v[4:7], v[172:175], v[212:215], v[4:7]
	v_mfma_f32_16x16x32_bf16 v[0:3], v[180:183], v[212:215], v[0:3]
	v_mfma_f32_16x16x32_bf16 v[52:55], v[176:179], v[192:195], v[52:55]
	v_mfma_f32_16x16x32_bf16 v[44:47], v[184:187], v[192:195], v[44:47]
	v_mfma_f32_16x16x32_bf16 v[36:39], v[176:179], v[200:203], v[36:39]
	v_mfma_f32_16x16x32_bf16 v[28:31], v[184:187], v[200:203], v[28:31]
	v_mfma_f32_16x16x32_bf16 v[20:23], v[176:179], v[208:211], v[20:23]
	v_mfma_f32_16x16x32_bf16 v[12:15], v[184:187], v[208:211], v[12:15]
	v_mfma_f32_16x16x32_bf16 v[4:7], v[176:179], v[216:219], v[4:7]
	v_mfma_f32_16x16x32_bf16 v[0:3], v[184:187], v[216:219], v[0:3]
	s_setprio 0
	s_barrier
	s_add_i32 s71, 0, 0x18000
	v_add_u32_e32 v129, s71, v160
	s_add_i32 s72, 0, 0x1c000
	ds_read_b128 v[130:133], v129
	ds_read_b128 v[134:137], v129 offset:1024
	ds_read_b128 v[138:141], v129 offset:2048
	ds_read_b128 v[168:171], v129 offset:3072
	v_add_u32_e32 v129, s72, v160
	ds_read_b128 v[172:175], v129
	ds_read_b128 v[176:179], v129 offset:1024
	ds_read_b128 v[180:183], v129 offset:2048
	ds_read_b128 v[184:187], v129 offset:3072
	s_add_u32 s100, s46, 0x80
	s_addc_u32 s101, s47, 0
	s_add_u32 s46, s46, 0x40000
	s_addc_u32 s47, s47, 0
	s_mov_b32 m0, s57
	ds_read_b128 v[188:191], v165 offset:32768
	ds_read_b128 v[192:195], v165 offset:33792
	ds_read_b128 v[196:199], v165 offset:34816
	ds_read_b128 v[200:203], v165 offset:35840
	ds_read_b128 v[204:207], v165 offset:36864
	ds_read_b128 v[208:211], v165 offset:37888
	ds_read_b128 v[212:215], v165 offset:38912
	ds_read_b128 v[216:219], v165 offset:39936
	global_load_lds_dwordx4 v146, s[46:47]
	s_mov_b32 m0, s58
	s_nop 0
	global_load_lds_dwordx4 v148, s[46:47]
	s_waitcnt vmcnt(8)
	s_waitcnt lgkmcnt(0)
	s_barrier
	s_setprio 1
	s_waitcnt lgkmcnt(0)
	v_mfma_f32_16x16x32_bf16 v[124:127], v[130:133], v[188:191], v[124:127]
	v_mfma_f32_16x16x32_bf16 v[120:123], v[138:141], v[188:191], v[120:123]
	v_mfma_f32_16x16x32_bf16 v[116:119], v[130:133], v[196:199], v[116:119]
	v_mfma_f32_16x16x32_bf16 v[112:115], v[138:141], v[196:199], v[112:115]
	v_mfma_f32_16x16x32_bf16 v[108:111], v[130:133], v[204:207], v[108:111]
	v_mfma_f32_16x16x32_bf16 v[100:103], v[138:141], v[204:207], v[100:103]
	v_mfma_f32_16x16x32_bf16 v[92:95], v[130:133], v[212:215], v[92:95]
	v_mfma_f32_16x16x32_bf16 v[84:87], v[138:141], v[212:215], v[84:87]
	v_mfma_f32_16x16x32_bf16 v[124:127], v[134:137], v[192:195], v[124:127]
	v_mfma_f32_16x16x32_bf16 v[120:123], v[168:171], v[192:195], v[120:123]
	v_mfma_f32_16x16x32_bf16 v[116:119], v[134:137], v[200:203], v[116:119]
	v_mfma_f32_16x16x32_bf16 v[112:115], v[168:171], v[200:203], v[112:115]
	v_mfma_f32_16x16x32_bf16 v[108:111], v[134:137], v[208:211], v[108:111]
	v_mfma_f32_16x16x32_bf16 v[100:103], v[168:171], v[208:211], v[100:103]
	v_mfma_f32_16x16x32_bf16 v[92:95], v[134:137], v[216:219], v[92:95]
	v_mfma_f32_16x16x32_bf16 v[84:87], v[168:171], v[216:219], v[84:87]
	s_setprio 0
	s_setprio 1
	v_mfma_f32_16x16x32_bf16 v[104:107], v[172:175], v[188:191], v[104:107]
	v_mfma_f32_16x16x32_bf16 v[96:99], v[180:183], v[188:191], v[96:99]
	v_mfma_f32_16x16x32_bf16 v[88:91], v[172:175], v[196:199], v[88:91]
	v_mfma_f32_16x16x32_bf16 v[80:83], v[180:183], v[196:199], v[80:83]
	v_mfma_f32_16x16x32_bf16 v[76:79], v[172:175], v[204:207], v[76:79]
	v_mfma_f32_16x16x32_bf16 v[72:75], v[180:183], v[204:207], v[72:75]
	v_mfma_f32_16x16x32_bf16 v[68:71], v[172:175], v[212:215], v[68:71]
	v_mfma_f32_16x16x32_bf16 v[64:67], v[180:183], v[212:215], v[64:67]
	v_mfma_f32_16x16x32_bf16 v[104:107], v[176:179], v[192:195], v[104:107]
	v_mfma_f32_16x16x32_bf16 v[96:99], v[184:187], v[192:195], v[96:99]
	v_mfma_f32_16x16x32_bf16 v[88:91], v[176:179], v[200:203], v[88:91]
	v_mfma_f32_16x16x32_bf16 v[80:83], v[184:187], v[200:203], v[80:83]
	v_mfma_f32_16x16x32_bf16 v[76:79], v[176:179], v[208:211], v[76:79]
	v_mfma_f32_16x16x32_bf16 v[72:75], v[184:187], v[208:211], v[72:75]
	v_mfma_f32_16x16x32_bf16 v[68:71], v[176:179], v[216:219], v[68:71]
	v_mfma_f32_16x16x32_bf16 v[64:67], v[184:187], v[216:219], v[64:67]
	s_setprio 0
	s_barrier
	s_add_i32 s46, s71, s56
	s_mov_b32 m0, s46
	ds_read_b128 v[188:191], v165 offset:49152
	ds_read_b128 v[192:195], v165 offset:50176
	ds_read_b128 v[196:199], v165 offset:51200
	ds_read_b128 v[200:203], v165 offset:52224
	ds_read_b128 v[204:207], v165 offset:53248
	ds_read_b128 v[208:211], v165 offset:54272
	ds_read_b128 v[212:215], v165 offset:55296
	ds_read_b128 v[216:219], v165 offset:56320
	s_add_u32 s98, s44, 0x80
	s_addc_u32 s99, s45, 0
	global_load_lds_dwordx4 v144, s[98:99]
	s_add_i32 m0, s46, 0x2000
	s_add_u32 s44, s44, 0x40080
	s_addc_u32 s45, s45, 0
	s_add_i32 s46, s72, s56
	global_load_lds_dwordx4 v150, s[98:99]
	s_mov_b32 m0, s46
	s_nop 0
	global_load_lds_dwordx4 v144, s[44:45]
	s_add_i32 m0, s46, 0x2000
	s_nop 0
	global_load_lds_dwordx4 v150, s[44:45]
	s_mov_b32 m0, s61
	s_nop 0
	global_load_lds_dwordx4 v146, s[100:101]
	s_mov_b32 m0, s62
	s_nop 0
	global_load_lds_dwordx4 v148, s[100:101]
	s_waitcnt vmcnt(8)
	s_waitcnt lgkmcnt(0)
	s_barrier
	s_setprio 1
	s_waitcnt lgkmcnt(0)
	v_mfma_f32_16x16x32_bf16 v[60:63], v[130:133], v[188:191], v[60:63]
	v_mfma_f32_16x16x32_bf16 v[56:59], v[138:141], v[188:191], v[56:59]
	v_mfma_f32_16x16x32_bf16 v[48:51], v[130:133], v[196:199], v[48:51]
	v_mfma_f32_16x16x32_bf16 v[40:43], v[138:141], v[196:199], v[40:43]
	v_mfma_f32_16x16x32_bf16 v[32:35], v[130:133], v[204:207], v[32:35]
	v_mfma_f32_16x16x32_bf16 v[24:27], v[138:141], v[204:207], v[24:27]
	v_mfma_f32_16x16x32_bf16 v[16:19], v[130:133], v[212:215], v[16:19]
	v_mfma_f32_16x16x32_bf16 v[8:11], v[138:141], v[212:215], v[8:11]
	v_mfma_f32_16x16x32_bf16 v[60:63], v[134:137], v[192:195], v[60:63]
	v_mfma_f32_16x16x32_bf16 v[56:59], v[168:171], v[192:195], v[56:59]
	v_mfma_f32_16x16x32_bf16 v[48:51], v[134:137], v[200:203], v[48:51]
	v_mfma_f32_16x16x32_bf16 v[40:43], v[168:171], v[200:203], v[40:43]
	v_mfma_f32_16x16x32_bf16 v[32:35], v[134:137], v[208:211], v[32:35]
	v_mfma_f32_16x16x32_bf16 v[24:27], v[168:171], v[208:211], v[24:27]
	v_mfma_f32_16x16x32_bf16 v[16:19], v[134:137], v[216:219], v[16:19]
	v_mfma_f32_16x16x32_bf16 v[8:11], v[168:171], v[216:219], v[8:11]
	s_setprio 0
	s_setprio 1
	v_mfma_f32_16x16x32_bf16 v[52:55], v[172:175], v[188:191], v[52:55]
	v_mfma_f32_16x16x32_bf16 v[44:47], v[180:183], v[188:191], v[44:47]
	v_mfma_f32_16x16x32_bf16 v[36:39], v[172:175], v[196:199], v[36:39]
	v_mfma_f32_16x16x32_bf16 v[28:31], v[180:183], v[196:199], v[28:31]
	v_mfma_f32_16x16x32_bf16 v[20:23], v[172:175], v[204:207], v[20:23]
	v_mfma_f32_16x16x32_bf16 v[12:15], v[180:183], v[204:207], v[12:15]
	v_mfma_f32_16x16x32_bf16 v[4:7], v[172:175], v[212:215], v[4:7]
	v_mfma_f32_16x16x32_bf16 v[0:3], v[180:183], v[212:215], v[0:3]
	v_mfma_f32_16x16x32_bf16 v[52:55], v[176:179], v[192:195], v[52:55]
	v_mfma_f32_16x16x32_bf16 v[44:47], v[184:187], v[192:195], v[44:47]
	v_mfma_f32_16x16x32_bf16 v[36:39], v[176:179], v[200:203], v[36:39]
	v_mfma_f32_16x16x32_bf16 v[28:31], v[184:187], v[200:203], v[28:31]
	v_mfma_f32_16x16x32_bf16 v[20:23], v[176:179], v[208:211], v[20:23]
	v_mfma_f32_16x16x32_bf16 v[12:15], v[184:187], v[208:211], v[12:15]
	v_mfma_f32_16x16x32_bf16 v[4:7], v[176:179], v[216:219], v[4:7]
	v_mfma_f32_16x16x32_bf16 v[0:3], v[184:187], v[216:219], v[0:3]
	s_setprio 0
	s_barrier
	s_add_i32 s70, s70, 2
	s_add_u32 s29, s29, 0x100
	s_addc_u32 s31, s31, 0
	s_add_u32 s42, s42, 0x100
	s_addc_u32 s43, s43, 0
	s_cmp_gt_u32 s70, 13
	s_cbranch_scc0 .LBB0_3651
	s_and_b64 vcc, exec, s[20:21]
	s_cbranch_vccz .LBB0_3654
	s_barrier
